# sec 7.5: RWKV scan step - each v_pk_fma_f32 that feeds the next MFMA's C operand split into two v_fma_f32 (bit-identical), 56 sites per layer
# baseline (speedup 1.0000x reference)
.LBB0_1305:
	s_lshl_b32 s2, s18, 11
	s_and_b32 s2, s2, 0x3000
	v_add_u32_e32 v202, s2, v177
	v_cvt_pk_bf16_f32 v162, v158, v159
	v_cvt_pk_bf16_f32 v163, v160, v161
	v_cvt_pk_bf16_f32 v164, v154, v155
	v_cvt_pk_bf16_f32 v165, v156, v157
	v_cvt_pk_bf16_f32 v166, v150, v151
	v_cvt_pk_bf16_f32 v167, v152, v153
	v_cvt_pk_bf16_f32 v168, v106, v107
	v_cvt_pk_bf16_f32 v169, v108, v109
	ds_write2st64_b64 v202, v[162:163], v[164:165] offset1:1
	ds_write2st64_b64 v202, v[166:167], v[168:169] offset0:2 offset1:3
	s_nop 1
	s_or_b32 s24, s18, 1
	v_mov_b32_e32 v222, s12
	v_add_u32_e32 v222, 0x10000, v222
	v_add_u32_e32 v231, 32, v222
	v_mov_b32_e32 v223, s24
	s_waitcnt vmcnt(45)
	v_lshlrev_b32_e32 v202, 16, v188
	v_and_b32_e32 v203, 0xffff0000, v188
	s_waitcnt vmcnt(44)
	v_fma_f32 v46, v158, v46, v202
	v_fma_f32 v47, v159, v47, v203
	v_lshlrev_b32_e32 v158, 16, v189
	v_and_b32_e32 v159, 0xffff0000, v189
	v_fma_f32 v48, v160, v48, v158
	v_fma_f32 v49, v161, v49, v159
	s_sub_i32 s2, 0x7c, s18
	s_add_i32 s10, s18, 3
	v_mfma_f32_16x16x32_bf16 v[38:41], v[38:41], v[162:165], v[46:49]
	s_and_b64 s[26:27], s[6:7], exec
	s_cselect_b32 s2, s10, s2
	s_add_i32 s26, s2, s19
	v_mfma_f32_16x16x32_bf16 v[158:161], v[30:33], v[166:169], v[38:41]
	s_waitcnt lgkmcnt(0)
	s_mov_b64 s[98:99], exec
	s_mov_b64 exec, s[0:1]
	ds_write_b32 v222, v223
	s_mov_b64 exec, s[98:99]
	ds_read_b32 v230, v231
	s_waitcnt vmcnt(41)
	v_lshlrev_b32_e32 v30, 16, v186
	v_and_b32_e32 v31, 0xffff0000, v186
	v_lshlrev_b32_e32 v32, 16, v187
	v_and_b32_e32 v33, 0xffff0000, v187
	s_waitcnt vmcnt(40)
	v_fma_f32 v30, v154, v42, v30
	v_fma_f32 v31, v155, v43, v31
	v_fma_f32 v32, v156, v44, v32
	v_fma_f32 v33, v157, v45, v33
	s_ashr_i32 s27, s26, 31
	s_lshl_b64 s[28:29], s[26:27], 13
	v_mfma_f32_16x16x32_bf16 v[18:21], v[18:21], v[162:165], v[30:33]
	s_add_u32 s30, s20, s28
	s_addc_u32 s31, s21, s29
	s_lshl_b64 s[26:27], s[26:27], 8
	v_mfma_f32_16x16x32_bf16 v[154:157], v[22:25], v[166:169], v[18:21]
	v_lshl_add_u64 v[30:31], v[178:179], 0, s[26:27]
	v_lshl_add_u64 v[32:33], v[180:181], 0, s[28:29]
	s_waitcnt vmcnt(37)
	s_nop 0
	v_lshlrev_b32_e32 v18, 16, v182
	v_and_b32_e32 v19, 0xffff0000, v182
	v_lshlrev_b32_e32 v20, 16, v183
	v_and_b32_e32 v21, 0xffff0000, v183
	s_waitcnt vmcnt(36)
	v_fma_f32 v18, v150, v26, v18
	v_fma_f32 v19, v151, v27, v19
	v_fma_f32 v20, v152, v28, v20
	v_fma_f32 v21, v153, v29, v21
	s_nop 1
	v_mfma_f32_16x16x32_bf16 v[2:5], v[2:5], v[162:165], v[18:21]
	v_mfma_f32_16x16x32_bf16 v[150:153], v[14:17], v[166:169], v[2:5]
	s_waitcnt vmcnt(33)
	s_nop 5
	v_lshlrev_b32_e32 v2, 16, v184
	v_and_b32_e32 v3, 0xffff0000, v184
	v_lshlrev_b32_e32 v4, 16, v185
	v_and_b32_e32 v5, 0xffff0000, v185
	s_waitcnt vmcnt(32)
	v_fma_f32 v2, v106, v34, v2
	v_fma_f32 v3, v107, v35, v3
	v_fma_f32 v4, v108, v36, v4
	v_fma_f32 v5, v109, v37, v5
	global_load_dwordx4 v[42:45], v174, s[30:31]
	global_load_dwordx4 v[34:37], v174, s[30:31] offset:1024
	v_mfma_f32_16x16x32_bf16 v[2:5], v[6:9], v[162:165], v[2:5]
	v_lshl_add_u64 v[6:7], s[30:31], 0, v[174:175]
	v_mfma_f32_16x16x32_bf16 v[106:109], v[10:13], v[166:169], v[2:5]
	v_add_co_u32_e32 v10, vcc, 0x1000, v6
	global_load_dwordx2 v[188:189], v[32:33], off
	global_load_dwordx4 v[46:49], v[30:31], off
	global_load_dwordx4 v[18:21], v174, s[30:31] offset:2048
	global_load_dwordx4 v[22:25], v174, s[30:31] offset:3072
	global_load_dwordx2 v[186:187], v[32:33], off offset:512
	global_load_dwordx4 v[38:41], v[30:31], off offset:64
	global_load_dwordx4 v[2:5], v206, s[30:31]
	v_addc_co_u32_e32 v11, vcc, 0, v7, vcc
	global_load_dwordx4 v[14:17], v[10:11], off offset:1024
	global_load_dwordx2 v[182:183], v[32:33], off offset:1024
	global_load_dwordx4 v[26:29], v[30:31], off offset:128
	global_load_dwordx4 v[6:9], v207, s[30:31]
	s_nop 0
	global_load_dwordx4 v[10:13], v[10:11], off offset:3072
	s_nop 0
	global_load_dwordx2 v[184:185], v[32:33], off offset:1536
	s_nop 0
	global_load_dwordx4 v[30:33], v[30:31], off offset:192
	s_andn2_b64 vcc, exec, s[8:9]
	s_cbranch_vccnz .LBB0_1310
	s_add_i32 s8, s12, 0
	s_add_i32 s8, s8, 0x10020
	s_waitcnt lgkmcnt(0)
	v_add_u32_e32 v162, 8, v230
	v_cmp_lt_u32_e32 vcc, s24, v162
	s_cbranch_vccnz .LBB0_1310

.LBB0_1310:
	s_lshl_b32 s2, s24, 11
	s_and_b32 s2, s2, 0x3800
	v_add_u32_e32 v202, s2, v177
	v_cvt_pk_bf16_f32 v162, v158, v159
	v_cvt_pk_bf16_f32 v163, v160, v161
	v_cvt_pk_bf16_f32 v164, v154, v155
	v_cvt_pk_bf16_f32 v165, v156, v157
	v_cvt_pk_bf16_f32 v166, v150, v151
	v_cvt_pk_bf16_f32 v167, v152, v153
	v_cvt_pk_bf16_f32 v168, v106, v107
	v_cvt_pk_bf16_f32 v169, v108, v109
	ds_write2st64_b64 v202, v[162:163], v[164:165] offset1:1
	ds_write2st64_b64 v202, v[166:167], v[168:169] offset0:2 offset1:3
	s_nop 1
	v_mov_b32_e32 v222, s12
	v_add_u32_e32 v222, 0x10000, v222
	v_add_u32_e32 v231, 32, v222
	v_mov_b32_e32 v223, s23
	s_waitcnt vmcnt(37)
	v_lshlrev_b32_e32 v202, 16, v196
	v_and_b32_e32 v203, 0xffff0000, v196
	s_waitcnt vmcnt(44)
	v_fma_f32 v94, v94, v158, v202
	v_fma_f32 v95, v95, v159, v203
	v_lshlrev_b32_e32 v158, 16, v197
	v_and_b32_e32 v159, 0xffff0000, v197
	v_fma_f32 v96, v96, v160, v158
	v_fma_f32 v97, v97, v161, v159
	s_sub_i32 s2, 0x7b, s18
	s_add_i32 s11, s18, 4
	v_mfma_f32_16x16x32_bf16 v[78:81], v[78:81], v[162:165], v[94:97]
	s_and_b64 s[8:9], s[6:7], exec
	s_cselect_b32 s2, s11, s2
	s_add_i32 s8, s2, s19
	v_mfma_f32_16x16x32_bf16 v[158:161], v[70:73], v[166:169], v[78:81]
	s_waitcnt lgkmcnt(0)
	s_mov_b64 s[98:99], exec
	s_mov_b64 exec, s[0:1]
	ds_write_b32 v222, v223
	s_mov_b64 exec, s[98:99]
	ds_read_b32 v230, v231
	s_waitcnt vmcnt(36)
	v_lshlrev_b32_e32 v70, 16, v194
	v_and_b32_e32 v71, 0xffff0000, v194
	v_lshlrev_b32_e32 v72, 16, v195
	v_and_b32_e32 v73, 0xffff0000, v195
	s_waitcnt vmcnt(40)
	v_fma_f32 v70, v82, v154, v70
	v_fma_f32 v71, v83, v155, v71
	v_fma_f32 v72, v84, v156, v72
	v_fma_f32 v73, v85, v157, v73
	s_ashr_i32 s9, s8, 31
	s_lshl_b64 s[24:25], s[8:9], 13
	v_mfma_f32_16x16x32_bf16 v[50:53], v[50:53], v[162:165], v[70:73]
	s_add_u32 s26, s20, s24
	s_addc_u32 s27, s21, s25
	s_lshl_b64 s[8:9], s[8:9], 8
	v_mfma_f32_16x16x32_bf16 v[94:97], v[58:61], v[166:169], v[50:53]
	s_cmp_lt_u32 s18, 6
	s_waitcnt vmcnt(35)
	s_nop 1
	v_lshlrev_b32_e32 v50, 16, v190
	v_and_b32_e32 v51, 0xffff0000, v190
	v_lshlrev_b32_e32 v52, 16, v191
	v_and_b32_e32 v53, 0xffff0000, v191
	s_waitcnt vmcnt(33)
	v_fma_f32 v50, v86, v150, v50
	v_fma_f32 v51, v87, v151, v51
	v_fma_f32 v52, v88, v152, v52
	v_fma_f32 v53, v89, v153, v53
	global_load_dwordx4 v[86:89], v174, s[26:27]
	global_load_dwordx4 v[78:81], v174, s[26:27] offset:1024
	v_mfma_f32_16x16x32_bf16 v[50:53], v[54:57], v[162:165], v[50:53]
	v_lshl_add_u64 v[54:55], s[26:27], 0, v[174:175]
	v_mfma_f32_16x16x32_bf16 v[150:153], v[74:77], v[166:169], v[50:53]
	v_lshl_add_u64 v[74:75], v[178:179], 0, s[8:9]
	v_lshl_add_u64 v[76:77], v[180:181], 0, s[24:25]
	s_waitcnt vmcnt(35)
	s_nop 2
	v_lshlrev_b32_e32 v50, 16, v192
	v_and_b32_e32 v51, 0xffff0000, v192
	v_lshlrev_b32_e32 v52, 16, v193
	v_and_b32_e32 v53, 0xffff0000, v193
	s_waitcnt vmcnt(34)
	v_fma_f32 v50, v90, v106, v50
	v_fma_f32 v51, v91, v107, v51
	v_fma_f32 v52, v92, v108, v52
	v_fma_f32 v53, v93, v109, v53
	v_add_co_u32_e32 v106, vcc, 0x1000, v54
	s_nop 0
	v_mfma_f32_16x16x32_bf16 v[50:53], v[62:65], v[162:165], v[50:53]
	v_addc_co_u32_e32 v107, vcc, 0, v55, vcc
	v_mfma_f32_16x16x32_bf16 v[154:157], v[66:69], v[166:169], v[50:53]
	global_load_dwordx2 v[196:197], v[76:77], off
	global_load_dwordx4 v[90:93], v[74:75], off
	global_load_dwordx4 v[62:65], v174, s[26:27] offset:2048
	global_load_dwordx4 v[66:69], v174, s[26:27] offset:3072
	global_load_dwordx2 v[194:195], v[76:77], off offset:512
	global_load_dwordx4 v[82:85], v[74:75], off offset:64
	global_load_dwordx4 v[50:53], v206, s[26:27]
	global_load_dwordx4 v[58:61], v[106:107], off offset:1024
	global_load_dwordx2 v[190:191], v[76:77], off offset:1024
	global_load_dwordx4 v[70:73], v[74:75], off offset:128
	global_load_dwordx4 v[54:57], v207, s[26:27]
	s_nop 0
	global_load_dwordx4 v[106:109], v[106:107], off offset:3072
	s_nop 0
	global_load_dwordx2 v[192:193], v[76:77], off offset:1536
	s_nop 0
	global_load_dwordx4 v[74:77], v[74:75], off offset:192
	s_cbranch_scc1 .LBB0_1315
	s_add_i32 s8, s12, 0
	s_add_i32 s8, s8, 0x10020
	s_waitcnt lgkmcnt(0)
	v_add_u32_e32 v162, 8, v230
	v_cmp_lt_u32_e32 vcc, s23, v162
	s_cbranch_vccnz .LBB0_1315

.LBB0_1315:
	s_lshl_b32 s2, s23, 11
	s_and_b32 s2, s2, 0x3000
	v_add_u32_e32 v202, s2, v177
	v_cvt_pk_bf16_f32 v162, v158, v159
	v_cvt_pk_bf16_f32 v163, v160, v161
	v_cvt_pk_bf16_f32 v164, v94, v95
	v_cvt_pk_bf16_f32 v165, v96, v97
	v_cvt_pk_bf16_f32 v166, v150, v151
	v_cvt_pk_bf16_f32 v167, v152, v153
	v_cvt_pk_bf16_f32 v168, v154, v155
	v_cvt_pk_bf16_f32 v169, v156, v157
	ds_write2st64_b64 v202, v[162:163], v[164:165] offset1:1
	ds_write2st64_b64 v202, v[166:167], v[168:169] offset0:2 offset1:3
	s_nop 1
	v_mov_b32_e32 v222, s12
	v_add_u32_e32 v222, 0x10000, v222
	v_add_u32_e32 v231, 32, v222
	v_mov_b32_e32 v223, s10
	s_waitcnt vmcnt(37)
	v_lshlrev_b32_e32 v202, 16, v200
	v_and_b32_e32 v203, 0xffff0000, v200
	v_fma_f32 v146, v146, v158, v202
	v_fma_f32 v147, v147, v159, v203
	v_lshlrev_b32_e32 v158, 16, v201
	v_and_b32_e32 v159, 0xffff0000, v201
	v_fma_f32 v148, v148, v160, v158
	v_fma_f32 v149, v149, v161, v159
	s_sub_i32 s2, 0x7a, s18
	s_add_i32 s23, s18, 5
	v_mfma_f32_16x16x32_bf16 v[142:145], v[142:145], v[162:165], v[146:149]
	s_and_b64 s[8:9], s[6:7], exec
	s_cselect_b32 s2, s23, s2
	s_add_i32 s8, s2, s19
	v_mfma_f32_16x16x32_bf16 v[158:161], v[138:141], v[166:169], v[142:145]
	s_waitcnt lgkmcnt(0)
	s_mov_b64 s[98:99], exec
	s_mov_b64 exec, s[0:1]
	ds_write_b32 v222, v223
	s_mov_b64 exec, s[98:99]
	ds_read_b32 v230, v231
	s_waitcnt vmcnt(36)
	v_lshlrev_b32_e32 v138, 16, v198
	v_and_b32_e32 v139, 0xffff0000, v198
	v_fma_f32 v94, v134, v94, v138
	v_fma_f32 v95, v135, v95, v139
	v_lshlrev_b32_e32 v134, 16, v199
	v_and_b32_e32 v135, 0xffff0000, v199
	v_fma_f32 v96, v136, v96, v134
	v_fma_f32 v97, v137, v97, v135
	s_ashr_i32 s9, s8, 31
	s_lshl_b64 s[24:25], s[8:9], 13
	v_mfma_f32_16x16x32_bf16 v[94:97], v[122:125], v[162:165], v[94:97]
	s_waitcnt vmcnt(35)
	v_lshlrev_b32_e32 v122, 16, v172
	v_and_b32_e32 v123, 0xffff0000, v172
	v_lshlrev_b32_e32 v124, 16, v173
	v_and_b32_e32 v125, 0xffff0000, v173
	s_waitcnt vmcnt(33)
	v_fma_f32 v122, v130, v150, v122
	v_fma_f32 v123, v131, v151, v123
	v_fma_f32 v124, v132, v152, v124
	v_fma_f32 v125, v133, v153, v125
	s_add_u32 s26, s20, s24
	s_addc_u32 s27, s21, s25
	v_mfma_f32_16x16x32_bf16 v[114:117], v[114:117], v[162:165], v[122:125]
	s_lshl_b64 s[8:9], s[8:9], 8
	v_lshl_add_u64 v[130:131], v[178:179], 0, s[8:9]
	v_lshl_add_u64 v[132:133], v[180:181], 0, s[24:25]
	v_mfma_f32_16x16x32_bf16 v[150:153], v[118:121], v[166:169], v[114:117]
	global_load_dwordx4 v[142:145], v174, s[26:27]
	global_load_dwordx4 v[134:137], v174, s[26:27] offset:1024
	s_cmp_lt_u32 s18, 5
	s_nop 0
	v_lshlrev_b32_e32 v114, 16, v170
	v_and_b32_e32 v115, 0xffff0000, v170
	s_waitcnt vmcnt(34)
	v_fma_f32 v110, v110, v154, v114
	v_fma_f32 v111, v111, v155, v115
	v_lshlrev_b32_e32 v114, 16, v171
	v_and_b32_e32 v115, 0xffff0000, v171
	v_fma_f32 v112, v112, v156, v114
	v_fma_f32 v113, v113, v157, v115
	v_mfma_f32_16x16x32_bf16 v[94:97], v[126:129], v[166:169], v[94:97]
	s_nop 0
	v_mfma_f32_16x16x32_bf16 v[98:101], v[98:101], v[162:165], v[110:113]
	v_mfma_f32_16x16x32_bf16 v[154:157], v[102:105], v[166:169], v[98:101]
	global_load_dwordx2 v[204:205], v[132:133], off
	global_load_dwordx4 v[146:149], v[130:131], off
	global_load_dwordx4 v[118:121], v174, s[26:27] offset:2048
	global_load_dwordx4 v[122:125], v174, s[26:27] offset:3072
	global_load_dwordx2 v[202:203], v[132:133], off offset:512
	global_load_dwordx4 v[138:141], v[130:131], off offset:64
	global_load_dwordx4 v[102:105], v206, s[26:27]
	v_lshl_add_u64 v[98:99], s[26:27], 0, v[174:175]
	v_add_co_u32_e32 v98, vcc, 0x1000, v98
	s_nop 1
	v_addc_co_u32_e32 v99, vcc, 0, v99, vcc
	global_load_dwordx4 v[114:117], v[98:99], off offset:1024
	global_load_dwordx2 v[198:199], v[132:133], off offset:1024
	global_load_dwordx4 v[126:129], v[130:131], off offset:128
	global_load_dwordx4 v[110:113], v207, s[26:27]
	s_nop 0
	global_load_dwordx4 v[98:101], v[98:99], off offset:3072
	s_nop 0
	global_load_dwordx2 v[200:201], v[132:133], off offset:1536
	s_nop 0
	global_load_dwordx4 v[130:133], v[130:131], off offset:192
	s_cbranch_scc1 .LBB0_1320
	s_add_i32 s8, s12, 0
	s_add_i32 s8, s8, 0x10020
	s_waitcnt lgkmcnt(0)
	v_add_u32_e32 v162, 8, v230
	v_cmp_lt_u32_e32 vcc, s10, v162
	s_cbranch_vccnz .LBB0_1320

.LBB0_1320:
	s_lshl_b32 s2, s10, 11
	s_and_b32 s2, s2, 0x3800
	v_add_u32_e32 v170, s2, v177
	v_cvt_pk_bf16_f32 v162, v158, v159
	v_cvt_pk_bf16_f32 v163, v160, v161
	v_cvt_pk_bf16_f32 v164, v94, v95
	v_cvt_pk_bf16_f32 v165, v96, v97
	v_cvt_pk_bf16_f32 v166, v150, v151
	v_cvt_pk_bf16_f32 v167, v152, v153
	v_cvt_pk_bf16_f32 v168, v154, v155
	v_cvt_pk_bf16_f32 v169, v156, v157
	ds_write2st64_b64 v170, v[162:163], v[164:165] offset1:1
	ds_write2st64_b64 v170, v[166:167], v[168:169] offset0:2 offset1:3
	s_nop 1
	v_mov_b32_e32 v222, s12
	v_add_u32_e32 v222, 0x10000, v222
	v_add_u32_e32 v231, 32, v222
	v_mov_b32_e32 v223, s11
	s_waitcnt vmcnt(45)
	v_lshlrev_b32_e32 v170, 16, v188
	v_and_b32_e32 v171, 0xffff0000, v188
	s_waitcnt vmcnt(44)
	v_fma_f32 v46, v46, v158, v170
	v_fma_f32 v47, v47, v159, v171
	v_lshlrev_b32_e32 v158, 16, v189
	v_and_b32_e32 v159, 0xffff0000, v189
	v_fma_f32 v48, v48, v160, v158
	v_fma_f32 v49, v49, v161, v159
	s_sub_i32 s2, 0x79, s18
	s_add_i32 s10, s18, 6
	v_mfma_f32_16x16x32_bf16 v[42:45], v[42:45], v[162:165], v[46:49]
	s_and_b64 s[8:9], s[6:7], exec
	s_cselect_b32 s2, s10, s2
	s_add_i32 s8, s2, s19
	v_mfma_f32_16x16x32_bf16 v[158:161], v[34:37], v[166:169], v[42:45]
	s_waitcnt lgkmcnt(0)
	s_mov_b64 s[98:99], exec
	s_mov_b64 exec, s[0:1]
	ds_write_b32 v222, v223
	s_mov_b64 exec, s[98:99]
	ds_read_b32 v230, v231
	s_waitcnt vmcnt(41)
	v_lshlrev_b32_e32 v34, 16, v186
	v_and_b32_e32 v35, 0xffff0000, v186
	v_lshlrev_b32_e32 v36, 16, v187
	v_and_b32_e32 v37, 0xffff0000, v187
	s_waitcnt vmcnt(40)
	v_fma_f32 v34, v38, v94, v34
	v_fma_f32 v35, v39, v95, v35
	v_fma_f32 v36, v40, v96, v36
	v_fma_f32 v37, v41, v97, v37
	s_ashr_i32 s9, s8, 31
	s_lshl_b64 s[24:25], s[8:9], 13
	v_mfma_f32_16x16x32_bf16 v[18:21], v[18:21], v[162:165], v[34:37]
	s_add_u32 s26, s20, s24
	s_addc_u32 s27, s21, s25
	s_lshl_b64 s[8:9], s[8:9], 8
	v_mfma_f32_16x16x32_bf16 v[94:97], v[22:25], v[166:169], v[18:21]
	v_lshl_add_u64 v[34:35], v[178:179], 0, s[8:9]
	v_lshl_add_u64 v[36:37], v[180:181], 0, s[24:25]
	s_cmp_lt_u32 s18, 4
	s_waitcnt vmcnt(37)
	v_lshlrev_b32_e32 v18, 16, v182
	v_and_b32_e32 v19, 0xffff0000, v182
	v_lshlrev_b32_e32 v20, 16, v183
	v_and_b32_e32 v21, 0xffff0000, v183
	s_waitcnt vmcnt(36)
	v_fma_f32 v18, v26, v150, v18
	v_fma_f32 v19, v27, v151, v19
	v_fma_f32 v20, v28, v152, v20
	v_fma_f32 v21, v29, v153, v21
	s_nop 1
	v_mfma_f32_16x16x32_bf16 v[2:5], v[2:5], v[162:165], v[18:21]
	v_mfma_f32_16x16x32_bf16 v[150:153], v[14:17], v[166:169], v[2:5]
	s_waitcnt vmcnt(33)
	s_nop 5
	v_lshlrev_b32_e32 v2, 16, v184
	v_and_b32_e32 v3, 0xffff0000, v184
	v_lshlrev_b32_e32 v4, 16, v185
	v_and_b32_e32 v5, 0xffff0000, v185
	s_waitcnt vmcnt(32)
	v_fma_f32 v2, v30, v154, v2
	v_fma_f32 v3, v31, v155, v3
	v_fma_f32 v4, v32, v156, v4
	v_fma_f32 v5, v33, v157, v5
	global_load_dwordx4 v[38:41], v174, s[26:27]
	global_load_dwordx4 v[30:33], v174, s[26:27] offset:1024
	v_mfma_f32_16x16x32_bf16 v[2:5], v[6:9], v[162:165], v[2:5]
	v_lshl_add_u64 v[6:7], s[26:27], 0, v[174:175]
	v_mfma_f32_16x16x32_bf16 v[154:157], v[10:13], v[166:169], v[2:5]
	v_add_co_u32_e32 v10, vcc, 0x1000, v6
	global_load_dwordx2 v[188:189], v[36:37], off
	global_load_dwordx4 v[46:49], v[34:35], off
	global_load_dwordx4 v[18:21], v174, s[26:27] offset:2048
	global_load_dwordx4 v[22:25], v174, s[26:27] offset:3072
	global_load_dwordx2 v[186:187], v[36:37], off offset:512
	global_load_dwordx4 v[42:45], v[34:35], off offset:64
	global_load_dwordx4 v[2:5], v206, s[26:27]
	v_addc_co_u32_e32 v11, vcc, 0, v7, vcc
	global_load_dwordx4 v[14:17], v[10:11], off offset:1024
	global_load_dwordx2 v[182:183], v[36:37], off offset:1024
	global_load_dwordx4 v[26:29], v[34:35], off offset:128
	global_load_dwordx4 v[6:9], v207, s[26:27]
	s_nop 0
	global_load_dwordx4 v[10:13], v[10:11], off offset:3072
	s_nop 0
	global_load_dwordx2 v[184:185], v[36:37], off offset:1536
	s_nop 0
	global_load_dwordx4 v[34:37], v[34:35], off offset:192
	s_cbranch_scc1 .LBB0_1325
	s_add_i32 s8, s12, 0
	s_add_i32 s8, s8, 0x10020
	s_waitcnt lgkmcnt(0)
	v_add_u32_e32 v162, 8, v230
	v_cmp_lt_u32_e32 vcc, s11, v162
	s_cbranch_vccnz .LBB0_1325

.LBB0_1325:
	s_lshl_b32 s2, s11, 11
	s_and_b32 s2, s2, 0x3000
	v_add_u32_e32 v162, s2, v177
	v_cvt_pk_bf16_f32 v170, v158, v159
	v_cvt_pk_bf16_f32 v171, v160, v161
	v_cvt_pk_bf16_f32 v172, v94, v95
	v_cvt_pk_bf16_f32 v173, v96, v97
	v_cvt_pk_bf16_f32 v166, v150, v151
	v_cvt_pk_bf16_f32 v167, v152, v153
	v_cvt_pk_bf16_f32 v168, v154, v155
	v_cvt_pk_bf16_f32 v169, v156, v157
	ds_write2st64_b64 v162, v[170:171], v[172:173] offset1:1
	ds_write2st64_b64 v162, v[166:167], v[168:169] offset0:2 offset1:3
	s_nop 1
	v_mov_b32_e32 v222, s12
	v_add_u32_e32 v222, 0x10000, v222
	v_add_u32_e32 v231, 32, v222
	v_mov_b32_e32 v223, s23
	s_waitcnt vmcnt(45)
	v_lshlrev_b32_e32 v162, 16, v196
	v_and_b32_e32 v163, 0xffff0000, v196
	s_waitcnt vmcnt(44)
	v_fma_f32 v90, v90, v158, v162
	v_fma_f32 v91, v91, v159, v163
	v_lshlrev_b32_e32 v158, 16, v197
	v_and_b32_e32 v159, 0xffff0000, v197
	v_fma_f32 v92, v92, v160, v158
	v_fma_f32 v93, v93, v161, v159
	s_sub_i32 s2, 0x78, s18
	s_add_i32 s3, s18, 7
	v_mfma_f32_16x16x32_bf16 v[86:89], v[86:89], v[170:173], v[90:93]
	s_and_b64 s[8:9], s[6:7], exec
	s_cselect_b32 s2, s3, s2
	s_add_i32 s8, s2, s19
	v_mfma_f32_16x16x32_bf16 v[158:161], v[78:81], v[166:169], v[86:89]
	s_waitcnt lgkmcnt(0)
	s_mov_b64 s[98:99], exec
	s_mov_b64 exec, s[0:1]
	ds_write_b32 v222, v223
	s_mov_b64 exec, s[98:99]
	ds_read_b32 v230, v231
	s_waitcnt vmcnt(41)
	v_lshlrev_b32_e32 v78, 16, v194
	v_and_b32_e32 v79, 0xffff0000, v194
	v_lshlrev_b32_e32 v80, 16, v195
	v_and_b32_e32 v81, 0xffff0000, v195
	s_waitcnt vmcnt(40)
	v_fma_f32 v78, v82, v94, v78
	v_fma_f32 v79, v83, v95, v79
	v_fma_f32 v80, v84, v96, v80
	v_fma_f32 v81, v85, v97, v81
	s_ashr_i32 s9, s8, 31
	s_lshl_b64 s[24:25], s[8:9], 13
	v_mfma_f32_16x16x32_bf16 v[62:65], v[62:65], v[170:173], v[78:81]
	s_add_u32 s26, s20, s24
	s_addc_u32 s27, s21, s25
	s_lshl_b64 s[8:9], s[8:9], 8
	v_mfma_f32_16x16x32_bf16 v[162:165], v[66:69], v[166:169], v[62:65]
	v_lshl_add_u64 v[90:91], v[178:179], 0, s[8:9]
	v_lshl_add_u64 v[86:87], v[180:181], 0, s[24:25]
	s_cmp_lt_u32 s18, 3
	s_waitcnt vmcnt(37)
	v_lshlrev_b32_e32 v62, 16, v190
	v_and_b32_e32 v63, 0xffff0000, v190
	v_lshlrev_b32_e32 v64, 16, v191
	v_and_b32_e32 v65, 0xffff0000, v191
	s_waitcnt vmcnt(36)
	v_fma_f32 v62, v70, v150, v62
	v_fma_f32 v63, v71, v151, v63
	v_fma_f32 v64, v72, v152, v64
	v_fma_f32 v65, v73, v153, v65
	global_load_dwordx4 v[78:81], v174, s[26:27]
	global_load_dwordx4 v[70:73], v174, s[26:27] offset:1024
	v_mfma_f32_16x16x32_bf16 v[50:53], v[50:53], v[170:173], v[62:65]
	v_mfma_f32_16x16x32_bf16 v[150:153], v[58:61], v[166:169], v[50:53]
	s_waitcnt vmcnt(35)
	s_nop 5
	v_lshlrev_b32_e32 v50, 16, v192
	v_and_b32_e32 v51, 0xffff0000, v192
	v_lshlrev_b32_e32 v52, 16, v193
	v_and_b32_e32 v53, 0xffff0000, v193
	s_waitcnt vmcnt(34)
	v_fma_f32 v50, v74, v154, v50
	v_fma_f32 v51, v75, v155, v51
	v_fma_f32 v52, v76, v156, v52
	v_fma_f32 v53, v77, v157, v53
	s_nop 1
	v_mfma_f32_16x16x32_bf16 v[154:157], v[54:57], v[170:173], v[50:53]
	v_lshl_add_u64 v[54:55], s[26:27], 0, v[174:175]
	v_add_co_u32_e32 v66, vcc, 0x1000, v54
	s_nop 0
	global_load_dwordx4 v[50:53], v174, s[26:27] offset:2048
	global_load_dwordx4 v[58:61], v174, s[26:27] offset:3072
	global_load_dwordx4 v[94:97], v[90:91], off
	global_load_dwordx4 v[82:85], v[90:91], off offset:64
	v_addc_co_u32_e32 v67, vcc, 0, v55, vcc
	global_load_dwordx4 v[54:57], v206, s[26:27]
	global_load_dwordx4 v[62:65], v207, s[26:27]
	global_load_dwordx4 v[74:77], v[66:67], off offset:1024
	s_nop 0
	global_load_dwordx4 v[66:69], v[66:67], off offset:3072
	s_nop 0
	global_load_dwordx2 v[196:197], v[86:87], off
	global_load_dwordx2 v[194:195], v[86:87], off offset:512
	global_load_dwordx2 v[190:191], v[86:87], off offset:1024
	global_load_dwordx2 v[192:193], v[86:87], off offset:1536
	s_nop 0
	global_load_dwordx4 v[86:89], v[90:91], off offset:128
	s_nop 0
	global_load_dwordx4 v[90:93], v[90:91], off offset:192
	v_mfma_f32_16x16x32_bf16 v[106:109], v[106:109], v[166:169], v[154:157]
	s_cbranch_scc1 .LBB0_1330
	s_add_i32 s8, s12, 0
	s_add_i32 s8, s8, 0x10020
	s_waitcnt lgkmcnt(0)
	v_add_u32_e32 v154, 8, v230
	v_cmp_lt_u32_e32 vcc, s23, v154
	s_cbranch_vccnz .LBB0_1330

.LBB0_1330:
	s_lshl_b32 s2, s23, 11
	s_and_b32 s2, s2, 0x3800
	v_add_u32_e32 v154, s2, v177
	v_cvt_pk_bf16_f32 v170, v158, v159
	v_cvt_pk_bf16_f32 v171, v160, v161
	v_cvt_pk_bf16_f32 v172, v162, v163
	v_cvt_pk_bf16_f32 v173, v164, v165
	v_cvt_pk_bf16_f32 v166, v150, v151
	v_cvt_pk_bf16_f32 v167, v152, v153
	v_cvt_pk_bf16_f32 v168, v106, v107
	v_cvt_pk_bf16_f32 v169, v108, v109
	ds_write2st64_b64 v154, v[170:171], v[172:173] offset1:1
	ds_write2st64_b64 v154, v[166:167], v[168:169] offset0:2 offset1:3
	s_nop 1
	v_mov_b32_e32 v222, s12
	v_add_u32_e32 v222, 0x10000, v222
	v_add_u32_e32 v231, 32, v222
	v_mov_b32_e32 v223, s10
	s_waitcnt vmcnt(45)
	v_lshlrev_b32_e32 v154, 16, v204
	v_and_b32_e32 v155, 0xffff0000, v204
	s_waitcnt vmcnt(44)
	v_fma_f32 v146, v146, v158, v154
	v_fma_f32 v147, v147, v159, v155
	v_lshlrev_b32_e32 v154, 16, v205
	v_and_b32_e32 v155, 0xffff0000, v205
	v_fma_f32 v148, v148, v160, v154
	v_fma_f32 v149, v149, v161, v155
	s_cmpk_lt_u32 s18, 0x78
	s_nop 0
	v_mfma_f32_16x16x32_bf16 v[142:145], v[142:145], v[170:173], v[146:149]
	v_mfma_f32_16x16x32_bf16 v[158:161], v[134:137], v[166:169], v[142:145]
	s_waitcnt lgkmcnt(0)
	s_mov_b64 s[98:99], exec
	s_mov_b64 exec, s[0:1]
	ds_write_b32 v222, v223
	s_mov_b64 exec, s[98:99]
	ds_read_b32 v230, v231
	s_waitcnt vmcnt(41)
	v_lshlrev_b32_e32 v134, 16, v202
	v_and_b32_e32 v135, 0xffff0000, v202
	v_lshlrev_b32_e32 v136, 16, v203
	v_and_b32_e32 v137, 0xffff0000, v203
	s_waitcnt vmcnt(40)
	v_fma_f32 v134, v138, v162, v134
	v_fma_f32 v135, v139, v163, v135
	v_fma_f32 v136, v140, v164, v136
	v_fma_f32 v137, v141, v165, v137
	s_nop 1
	v_mfma_f32_16x16x32_bf16 v[118:121], v[118:121], v[170:173], v[134:137]
	v_mfma_f32_16x16x32_bf16 v[154:157], v[122:125], v[166:169], v[118:121]
	s_waitcnt vmcnt(37)
	s_nop 5
	v_lshlrev_b32_e32 v118, 16, v198
	v_and_b32_e32 v119, 0xffff0000, v198
	v_lshlrev_b32_e32 v120, 16, v199
	v_and_b32_e32 v121, 0xffff0000, v199
	s_waitcnt vmcnt(36)
	v_fma_f32 v118, v126, v150, v118
	v_fma_f32 v119, v127, v151, v119
	v_fma_f32 v120, v128, v152, v120
	v_fma_f32 v121, v129, v153, v121
	s_nop 1
	v_mfma_f32_16x16x32_bf16 v[102:105], v[102:105], v[170:173], v[118:121]
	v_mfma_f32_16x16x32_bf16 v[150:153], v[114:117], v[166:169], v[102:105]
	s_waitcnt vmcnt(33)
	s_nop 5
	v_lshlrev_b32_e32 v102, 16, v200
	v_and_b32_e32 v103, 0xffff0000, v200
	v_lshlrev_b32_e32 v104, 16, v201
	v_and_b32_e32 v105, 0xffff0000, v201
	s_waitcnt vmcnt(32)
	v_fma_f32 v102, v130, v106, v102
	v_fma_f32 v103, v131, v107, v103
	v_fma_f32 v104, v132, v108, v104
	v_fma_f32 v105, v133, v109, v105
	s_nop 1
	v_mfma_f32_16x16x32_bf16 v[102:105], v[110:113], v[170:173], v[102:105]
	v_mfma_f32_16x16x32_bf16 v[106:109], v[98:101], v[166:169], v[102:105]
	s_cbranch_scc0 .LBB0_1334
	s_mov_b32 s18, s10
	s_branch .LBB0_1302

.LBB0_1337:
	v_cvt_pk_bf16_f32 v50, v158, v159
	v_cvt_pk_bf16_f32 v51, v160, v161
	v_cvt_pk_bf16_f32 v52, v154, v155
	v_cvt_pk_bf16_f32 v53, v156, v157
	s_waitcnt vmcnt(9)
	v_cvt_pk_bf16_f32 v54, v150, v151
	v_cvt_pk_bf16_f32 v55, v152, v153
	v_cvt_pk_bf16_f32 v56, v106, v107
	v_cvt_pk_bf16_f32 v57, v108, v109
	ds_write2st64_b64 v177, v[50:51], v[52:53] offset0:24 offset1:25
	ds_write2st64_b64 v177, v[54:55], v[56:57] offset0:26 offset1:27
	s_waitcnt lgkmcnt(0)
	s_and_saveexec_b64 s[6:7], s[0:1]
	s_add_i32 s2, s8, 0x10000
	v_mov_b32_e32 v58, 0x7f
	v_mov_b32_e32 v59, s2
	ds_write_b32 v59, v58
	s_or_b64 exec, exec, s[6:7]
	v_lshlrev_b32_e32 v58, 16, v188
	v_and_b32_e32 v59, 0xffff0000, v188
	v_fma_f32 v46, v46, v158, v58
	v_fma_f32 v47, v47, v159, v59
	v_lshlrev_b32_e32 v58, 16, v189
	v_and_b32_e32 v59, 0xffff0000, v189
	v_fma_f32 v48, v48, v160, v58
	v_fma_f32 v49, v49, v161, v59
	s_movk_i32 s2, 0xff80
	s_nop 0
	v_mfma_f32_16x16x32_bf16 v[38:41], v[38:41], v[50:53], v[46:49]
	v_mfma_f32_16x16x32_bf16 v[30:33], v[30:33], v[54:57], v[38:41]
	s_nop 6
	v_lshlrev_b32_e32 v38, 16, v186
	v_and_b32_e32 v39, 0xffff0000, v186
	v_lshlrev_b32_e32 v40, 16, v187
	v_and_b32_e32 v41, 0xffff0000, v187
	v_fma_f32 v38, v42, v154, v38
	v_fma_f32 v39, v43, v155, v39
	v_fma_f32 v40, v44, v156, v40
	v_fma_f32 v41, v45, v157, v41
	s_nop 1
	v_mfma_f32_16x16x32_bf16 v[18:21], v[18:21], v[50:53], v[38:41]
	v_mfma_f32_16x16x32_bf16 v[18:21], v[22:25], v[54:57], v[18:21]
	v_lshlrev_b32_e32 v22, 16, v182
	v_and_b32_e32 v23, 0xffff0000, v182
	v_lshlrev_b32_e32 v24, 16, v183
	v_and_b32_e32 v25, 0xffff0000, v183
	v_fma_f32 v22, v26, v150, v22
	v_fma_f32 v23, v27, v151, v23
	v_fma_f32 v24, v28, v152, v24
	v_fma_f32 v25, v29, v153, v25
	s_nop 1
	v_mfma_f32_16x16x32_bf16 v[2:5], v[2:5], v[50:53], v[22:25]
	v_mfma_f32_16x16x32_bf16 v[2:5], v[14:17], v[54:57], v[2:5]
	v_mov_b32_e32 v16, s9
	v_lshlrev_b32_e32 v14, 16, v184
	v_and_b32_e32 v15, 0xffff0000, v184
	ds_read_b32 v22, v16
	v_lshlrev_b32_e32 v16, 16, v185
	v_and_b32_e32 v17, 0xffff0000, v185
	v_fma_f32 v14, v34, v106, v14
	v_fma_f32 v15, v35, v107, v15
	v_fma_f32 v16, v36, v108, v16
	v_fma_f32 v17, v37, v109, v17
	s_nop 1
	v_mfma_f32_16x16x32_bf16 v[6:9], v[6:9], v[50:53], v[14:17]
	v_mfma_f32_16x16x32_bf16 v[6:9], v[10:13], v[54:57], v[6:9]
	s_waitcnt lgkmcnt(0)
	s_nop 0
	v_add_u32_e32 v14, 0xffffff88, v22
	v_cmp_gt_u32_e32 vcc, s2, v14
	s_cbranch_vccnz .LBB0_1342
	s_movk_i32 s2, 0xff7f

.LBB0_3623:
	s_lshl_b32 s2, s20, 11
	s_and_b32 s2, s2, 0x3000
	v_add_u32_e32 v162, s2, v189
	v_cvt_pk_bf16_f32 v174, v154, v155
	v_cvt_pk_bf16_f32 v175, v156, v157
	v_cvt_pk_bf16_f32 v176, v150, v151
	v_cvt_pk_bf16_f32 v177, v152, v153
	v_cvt_pk_bf16_f32 v178, v102, v103
	v_cvt_pk_bf16_f32 v179, v104, v105
	v_cvt_pk_bf16_f32 v180, v106, v107
	v_cvt_pk_bf16_f32 v181, v108, v109
	ds_write2st64_b64 v162, v[174:175], v[176:177] offset1:1
	ds_write2st64_b64 v162, v[178:179], v[180:181] offset0:2 offset1:3
	s_nop 1
	s_or_b32 s17, s20, 1
	v_mov_b32_e32 v222, s9
	v_add_u32_e32 v222, 0x10000, v222
	v_add_u32_e32 v231, 32, v222
	v_mov_b32_e32 v223, s17
	s_waitcnt vmcnt(37)
	v_lshlrev_b32_e32 v162, 16, v196
	v_and_b32_e32 v163, 0xffff0000, v196
	v_fma_f32 v46, v154, v46, v162
	v_fma_f32 v47, v155, v47, v163
	v_lshlrev_b32_e32 v154, 16, v197
	v_and_b32_e32 v155, 0xffff0000, v197
	v_fma_f32 v48, v156, v48, v154
	v_fma_f32 v49, v157, v49, v155
	s_sub_i32 s15, 0x7c, s20
	s_add_i32 s14, s20, 3
	v_mfma_f32_16x16x32_bf16 v[42:45], v[42:45], v[174:177], v[46:49]
	s_and_b64 s[2:3], s[6:7], exec
	s_cselect_b32 s2, s14, s15
	s_add_i32 s2, s2, s21
	v_mfma_f32_16x16x32_bf16 v[170:173], v[34:37], v[178:181], v[42:45]
	s_waitcnt lgkmcnt(0)
	s_mov_b64 s[98:99], exec
	s_mov_b64 exec, s[0:1]
	ds_write_b32 v222, v223
	s_mov_b64 exec, s[98:99]
	ds_read_b32 v230, v231
	s_waitcnt vmcnt(36)
	v_lshlrev_b32_e32 v34, 16, v184
	v_and_b32_e32 v35, 0xffff0000, v184
	v_fma_f32 v26, v150, v26, v34
	v_fma_f32 v27, v151, v27, v35
	v_lshlrev_b32_e32 v34, 16, v185
	v_and_b32_e32 v35, 0xffff0000, v185
	v_fma_f32 v28, v152, v28, v34
	v_fma_f32 v29, v153, v29, v35
	s_ashr_i32 s3, s2, 31
	s_lshl_b64 s[26:27], s[2:3], 13
	v_mfma_f32_16x16x32_bf16 v[18:21], v[18:21], v[174:177], v[26:29]
	s_add_u32 s28, s22, s26
	s_addc_u32 s29, s23, s27
	s_lshl_b64 s[2:3], s[2:3], 8
	v_mfma_f32_16x16x32_bf16 v[166:169], v[22:25], v[178:181], v[18:21]
	v_lshl_add_u64 v[22:23], v[190:191], 0, s[2:3]
	v_lshl_add_u64 v[24:25], v[192:193], 0, s[26:27]
	global_load_dwordx4 v[154:157], v186, s[28:29]
	global_load_dwordx4 v[150:153], v186, s[28:29] offset:1024
	s_waitcnt vmcnt(37)
	v_lshlrev_b32_e32 v18, 16, v182
	v_and_b32_e32 v19, 0xffff0000, v182
	v_lshlrev_b32_e32 v20, 16, v183
	v_and_b32_e32 v21, 0xffff0000, v183
	s_waitcnt vmcnt(35)
	v_fma_f32 v18, v102, v30, v18
	v_fma_f32 v19, v103, v31, v19
	v_fma_f32 v20, v104, v32, v20
	v_fma_f32 v21, v105, v33, v21
	s_waitcnt vmcnt(29)
	s_nop 0
	v_mfma_f32_16x16x32_bf16 v[182:185], v[38:41], v[174:177], v[18:21]
	global_load_dwordx4 v[34:37], v186, s[28:29] offset:2048
	global_load_dwordx4 v[38:41], v186, s[28:29] offset:3072
	global_load_dwordx4 v[162:165], v[22:23], off
	global_load_dwordx4 v[46:49], v[22:23], off offset:64
	v_lshl_add_u64 v[18:19], s[28:29], 0, v[186:187]
	v_add_co_u32_e32 v42, vcc, 0x1000, v18
	v_mfma_f32_16x16x32_bf16 v[182:185], v[10:13], v[178:181], v[182:185]
	s_nop 0
	v_addc_co_u32_e32 v43, vcc, 0, v19, vcc
	global_load_dwordx4 v[26:29], v220, s[28:29]
	global_load_dwordx4 v[18:21], v221, s[28:29]
	global_load_dwordx4 v[30:33], v[42:43], off offset:1024
	global_load_dwordx4 v[102:105], v[42:43], off offset:3072
	global_load_dwordx2 v[218:219], v[24:25], off
	global_load_dwordx2 v[214:215], v[24:25], off offset:512
	global_load_dwordx2 v[210:211], v[24:25], off offset:1024
	global_load_dwordx2 v[196:197], v[24:25], off offset:1536
	s_nop 0
	global_load_dwordx4 v[42:45], v[22:23], off offset:128
	s_nop 0
	global_load_dwordx4 v[22:25], v[22:23], off offset:192
	v_lshlrev_b32_e32 v10, 16, v194
	v_and_b32_e32 v11, 0xffff0000, v194
	v_fma_f32 v6, v106, v6, v10
	v_fma_f32 v7, v107, v7, v11
	v_lshlrev_b32_e32 v10, 16, v195
	v_and_b32_e32 v11, 0xffff0000, v195
	v_fma_f32 v8, v108, v8, v10
	v_fma_f32 v9, v109, v9, v11
	s_andn2_b64 vcc, exec, s[12:13]
	s_waitcnt vmcnt(41)
	v_mfma_f32_16x16x32_bf16 v[6:9], v[14:17], v[174:177], v[6:9]
	v_mfma_f32_16x16x32_bf16 v[106:109], v[2:5], v[178:181], v[6:9]
	s_cbranch_vccnz .LBB0_3628
	s_add_i32 s12, s9, 0
	s_add_i32 s12, s12, 0x10020
	s_waitcnt lgkmcnt(0)
	v_add_u32_e32 v2, 8, v230
	v_cmp_lt_u32_e32 vcc, s17, v2
	s_cbranch_vccnz .LBB0_3628

.LBB0_3628:
	s_lshl_b32 s2, s17, 11
	s_and_b32 s2, s2, 0x3800
	v_add_u32_e32 v2, s2, v189
	v_cvt_pk_bf16_f32 v174, v170, v171
	v_cvt_pk_bf16_f32 v175, v172, v173
	v_cvt_pk_bf16_f32 v176, v166, v167
	v_cvt_pk_bf16_f32 v177, v168, v169
	v_cvt_pk_bf16_f32 v14, v182, v183
	v_cvt_pk_bf16_f32 v15, v184, v185
	v_cvt_pk_bf16_f32 v16, v106, v107
	v_cvt_pk_bf16_f32 v17, v108, v109
	ds_write2st64_b64 v2, v[174:175], v[176:177] offset1:1
	ds_write2st64_b64 v2, v[14:15], v[16:17] offset0:2 offset1:3
	s_nop 1
	v_mov_b32_e32 v222, s9
	v_add_u32_e32 v222, 0x10000, v222
	v_add_u32_e32 v231, 32, v222
	v_mov_b32_e32 v223, s16
	s_waitcnt vmcnt(37)
	v_lshlrev_b32_e32 v2, 16, v204
	v_and_b32_e32 v3, 0xffff0000, v204
	v_lshlrev_b32_e32 v4, 16, v205
	v_and_b32_e32 v5, 0xffff0000, v205
	v_fma_f32 v2, v94, v170, v2
	v_fma_f32 v3, v95, v171, v3
	v_fma_f32 v4, v96, v172, v4
	v_fma_f32 v5, v97, v173, v5
	s_sub_i32 s12, 0x7b, s20
	s_add_i32 s15, s20, 4
	v_mfma_f32_16x16x32_bf16 v[2:5], v[86:89], v[174:177], v[2:5]
	s_and_b64 s[2:3], s[6:7], exec
	s_cselect_b32 s2, s15, s12
	s_add_i32 s2, s2, s21
	s_waitcnt vmcnt(35)
	v_lshlrev_b32_e32 v6, 16, v200
	v_and_b32_e32 v7, 0xffff0000, v200
	v_lshlrev_b32_e32 v8, 16, v201
	v_and_b32_e32 v9, 0xffff0000, v201
	s_ashr_i32 s3, s2, 31
	v_mfma_f32_16x16x32_bf16 v[10:13], v[78:81], v[14:17], v[2:5]
	s_waitcnt lgkmcnt(0)
	s_mov_b64 s[98:99], exec
	s_mov_b64 exec, s[0:1]
	ds_write_b32 v222, v223
	s_mov_b64 exec, s[98:99]
	ds_read_b32 v230, v231
	s_waitcnt vmcnt(33)
	v_fma_f32 v6, v90, v182, v6
	v_fma_f32 v7, v91, v183, v7
	v_fma_f32 v8, v92, v184, v8
	v_fma_f32 v9, v93, v185, v9
	s_lshl_b64 s[12:13], s[2:3], 13
	v_lshlrev_b32_e32 v2, 16, v202
	v_and_b32_e32 v3, 0xffff0000, v202
	v_lshlrev_b32_e32 v4, 16, v203
	v_and_b32_e32 v5, 0xffff0000, v203
	v_fma_f32 v2, v82, v166, v2
	v_fma_f32 v3, v83, v167, v3
	v_fma_f32 v4, v84, v168, v4
	v_fma_f32 v5, v85, v169, v5
	v_mfma_f32_16x16x32_bf16 v[6:9], v[58:61], v[174:177], v[6:9]
	v_lshlrev_b32_e32 v58, 16, v198
	v_and_b32_e32 v59, 0xffff0000, v198
	v_lshlrev_b32_e32 v60, 16, v199
	v_and_b32_e32 v61, 0xffff0000, v199
	s_add_u32 s26, s22, s12
	v_mfma_f32_16x16x32_bf16 v[2:5], v[62:65], v[174:177], v[2:5]
	s_waitcnt vmcnt(32)
	v_fma_f32 v58, v74, v106, v58
	v_fma_f32 v59, v75, v107, v59
	v_fma_f32 v60, v76, v108, v60
	v_fma_f32 v61, v77, v109, v61
	s_addc_u32 s27, s23, s13
	s_lshl_b64 s[2:3], s[2:3], 8
	v_mfma_f32_16x16x32_bf16 v[166:169], v[54:57], v[174:177], v[58:61]
	v_lshl_add_u64 v[54:55], s[26:27], 0, v[186:187]
	v_add_co_u32_e32 v78, vcc, 0x1000, v54
	s_nop 0
	v_lshl_add_u64 v[58:59], v[190:191], 0, s[2:3]
	v_lshl_add_u64 v[60:61], v[192:193], 0, s[12:13]
	v_addc_co_u32_e32 v79, vcc, 0, v55, vcc
	v_mfma_f32_16x16x32_bf16 v[2:5], v[66:69], v[14:17], v[2:5]
	global_load_dwordx4 v[90:93], v186, s[26:27]
	global_load_dwordx4 v[86:89], v186, s[26:27] offset:1024
	s_cmp_lt_u32 s20, 6
	v_mfma_f32_16x16x32_bf16 v[6:9], v[70:73], v[14:17], v[6:9]
	global_load_dwordx4 v[70:73], v186, s[26:27] offset:2048
	global_load_dwordx4 v[74:77], v186, s[26:27] offset:3072
	global_load_dwordx4 v[94:97], v[58:59], off
	global_load_dwordx4 v[82:85], v[58:59], off offset:64
	global_load_dwordx4 v[62:65], v220, s[26:27]
	global_load_dwordx4 v[54:57], v221, s[26:27]
	global_load_dwordx4 v[66:69], v[78:79], off offset:1024
	global_load_dwordx4 v[106:109], v[78:79], off offset:3072
	global_load_dwordx2 v[202:203], v[60:61], off
	global_load_dwordx2 v[200:201], v[60:61], off offset:512
	global_load_dwordx2 v[198:199], v[60:61], off offset:1024
	global_load_dwordx2 v[178:179], v[60:61], off offset:1536
	s_nop 0
	global_load_dwordx4 v[78:81], v[58:59], off offset:128
	s_nop 0
	global_load_dwordx4 v[58:61], v[58:59], off offset:192
	v_mfma_f32_16x16x32_bf16 v[50:53], v[50:53], v[14:17], v[166:169]
	s_cbranch_scc1 .LBB0_3633
	s_add_i32 s12, s9, 0
	s_add_i32 s12, s12, 0x10020
	s_waitcnt lgkmcnt(0)
	v_add_u32_e32 v14, 8, v230
	v_cmp_lt_u32_e32 vcc, s16, v14
	s_cbranch_vccnz .LBB0_3633

.LBB0_3633:
	s_lshl_b32 s2, s16, 11
	s_and_b32 s2, s2, 0x3000
	v_add_u32_e32 v170, s2, v189
	v_cvt_pk_bf16_f32 v166, v10, v11
	v_cvt_pk_bf16_f32 v167, v12, v13
	v_cvt_pk_bf16_f32 v168, v2, v3
	v_cvt_pk_bf16_f32 v169, v4, v5
	v_cvt_pk_bf16_f32 v14, v6, v7
	v_cvt_pk_bf16_f32 v15, v8, v9
	v_cvt_pk_bf16_f32 v16, v50, v51
	v_cvt_pk_bf16_f32 v17, v52, v53
	ds_write2st64_b64 v170, v[166:167], v[168:169] offset1:1
	ds_write2st64_b64 v170, v[14:15], v[16:17] offset0:2 offset1:3
	s_nop 1
	v_mov_b32_e32 v222, s9
	v_add_u32_e32 v222, 0x10000, v222
	v_add_u32_e32 v231, 32, v222
	v_mov_b32_e32 v223, s14
	s_waitcnt vmcnt(37)
	v_lshlrev_b32_e32 v170, 16, v216
	v_and_b32_e32 v171, 0xffff0000, v216
	v_fma_f32 v10, v158, v10, v170
	v_fma_f32 v11, v159, v11, v171
	v_lshlrev_b32_e32 v158, 16, v217
	v_and_b32_e32 v159, 0xffff0000, v217
	v_fma_f32 v12, v160, v12, v158
	v_fma_f32 v13, v161, v13, v159
	s_sub_i32 s12, 0x7a, s20
	s_add_i32 s16, s20, 5
	v_mfma_f32_16x16x32_bf16 v[10:13], v[146:149], v[166:169], v[10:13]
	s_and_b64 s[2:3], s[6:7], exec
	s_cselect_b32 s2, s16, s12
	s_add_i32 s2, s2, s21
	v_mfma_f32_16x16x32_bf16 v[10:13], v[142:145], v[14:17], v[10:13]
	s_waitcnt lgkmcnt(0)
	s_mov_b64 s[98:99], exec
	s_mov_b64 exec, s[0:1]
	ds_write_b32 v222, v223
	s_mov_b64 exec, s[98:99]
	ds_read_b32 v230, v231
	s_waitcnt vmcnt(36)
	v_lshlrev_b32_e32 v142, 16, v212
	v_and_b32_e32 v143, 0xffff0000, v212
	v_fma_f32 v2, v138, v2, v142
	v_fma_f32 v3, v139, v3, v143
	v_lshlrev_b32_e32 v138, 16, v213
	v_and_b32_e32 v139, 0xffff0000, v213
	v_fma_f32 v4, v140, v4, v138
	v_fma_f32 v5, v141, v5, v139
	s_ashr_i32 s3, s2, 31
	s_lshl_b64 s[12:13], s[2:3], 13
	v_mfma_f32_16x16x32_bf16 v[2:5], v[126:129], v[166:169], v[2:5]
	s_waitcnt vmcnt(35)
	v_lshlrev_b32_e32 v126, 16, v208
	v_and_b32_e32 v127, 0xffff0000, v208
	s_waitcnt vmcnt(33)
	v_fma_f32 v6, v134, v6, v126
	v_fma_f32 v7, v135, v7, v127
	v_lshlrev_b32_e32 v126, 16, v209
	v_and_b32_e32 v127, 0xffff0000, v209
	v_fma_f32 v8, v136, v8, v126
	v_fma_f32 v9, v137, v9, v127
	s_add_u32 s26, s22, s12
	s_addc_u32 s27, s23, s13
	v_mfma_f32_16x16x32_bf16 v[6:9], v[118:121], v[166:169], v[6:9]
	v_lshlrev_b32_e32 v118, 16, v206
	v_and_b32_e32 v119, 0xffff0000, v206
	s_waitcnt vmcnt(32)
	v_fma_f32 v50, v114, v50, v118
	v_fma_f32 v51, v115, v51, v119
	v_lshlrev_b32_e32 v114, 16, v207
	v_and_b32_e32 v115, 0xffff0000, v207
	v_fma_f32 v52, v116, v52, v114
	v_fma_f32 v53, v117, v53, v115
	s_lshl_b64 s[2:3], s[2:3], 8
	v_lshl_add_u64 v[118:119], v[190:191], 0, s[2:3]
	v_mfma_f32_16x16x32_bf16 v[50:53], v[110:113], v[166:169], v[50:53]
	v_lshl_add_u64 v[110:111], s[26:27], 0, v[186:187]
	v_add_co_u32_e32 v110, vcc, 0x1000, v110
	v_lshl_add_u64 v[120:121], v[192:193], 0, s[12:13]
	s_nop 0
	v_addc_co_u32_e32 v111, vcc, 0, v111, vcc
	v_mfma_f32_16x16x32_bf16 v[2:5], v[130:133], v[14:17], v[2:5]
	global_load_dwordx4 v[158:161], v186, s[26:27]
	global_load_dwordx4 v[146:149], v186, s[26:27] offset:1024
	global_load_dwordx4 v[130:133], v186, s[26:27] offset:2048
	global_load_dwordx4 v[134:137], v186, s[26:27] offset:3072
	global_load_dwordx4 v[166:169], v[118:119], off
	global_load_dwordx4 v[142:145], v[118:119], off offset:64
	s_cmp_lt_u32 s20, 5
	v_mfma_f32_16x16x32_bf16 v[6:9], v[122:125], v[14:17], v[6:9]
	global_load_dwordx4 v[122:125], v220, s[26:27]
	global_load_dwordx4 v[114:117], v221, s[26:27]
	global_load_dwordx4 v[126:129], v[110:111], off offset:1024
	s_nop 0
	global_load_dwordx4 v[110:113], v[110:111], off offset:3072
	s_nop 0
	global_load_dwordx2 v[212:213], v[120:121], off
	global_load_dwordx2 v[208:209], v[120:121], off offset:512
	global_load_dwordx2 v[206:207], v[120:121], off offset:1024
	global_load_dwordx2 v[180:181], v[120:121], off offset:1536
	global_load_dwordx4 v[138:141], v[118:119], off offset:128
	s_nop 0
	global_load_dwordx4 v[118:121], v[118:119], off offset:192
	v_mfma_f32_16x16x32_bf16 v[14:17], v[98:101], v[14:17], v[50:53]
	s_cbranch_scc1 .LBB0_3638
	s_add_i32 s12, s9, 0
	s_add_i32 s12, s12, 0x10020
	s_waitcnt lgkmcnt(0)
	v_add_u32_e32 v50, 8, v230
	v_cmp_lt_u32_e32 vcc, s14, v50
	s_cbranch_vccnz .LBB0_3638

.LBB0_3638:
	s_lshl_b32 s2, s14, 11
	s_and_b32 s2, s2, 0x3800
	v_add_u32_e32 v50, s2, v189
	v_cvt_pk_bf16_f32 v174, v10, v11
	v_cvt_pk_bf16_f32 v175, v12, v13
	v_cvt_pk_bf16_f32 v176, v2, v3
	v_cvt_pk_bf16_f32 v177, v4, v5
	v_cvt_pk_bf16_f32 v170, v6, v7
	v_cvt_pk_bf16_f32 v171, v8, v9
	v_cvt_pk_bf16_f32 v172, v14, v15
	v_cvt_pk_bf16_f32 v173, v16, v17
	ds_write2st64_b64 v50, v[174:175], v[176:177] offset1:1
	ds_write2st64_b64 v50, v[170:171], v[172:173] offset0:2 offset1:3
	s_nop 1
	v_mov_b32_e32 v222, s9
	v_add_u32_e32 v222, 0x10000, v222
	v_add_u32_e32 v231, 32, v222
	v_mov_b32_e32 v223, s15
	s_waitcnt vmcnt(37)
	v_lshlrev_b32_e32 v50, 16, v218
	v_and_b32_e32 v51, 0xffff0000, v218
	v_fma_f32 v10, v162, v10, v50
	v_fma_f32 v11, v163, v11, v51
	v_lshlrev_b32_e32 v50, 16, v219
	v_and_b32_e32 v51, 0xffff0000, v219
	v_fma_f32 v12, v164, v12, v50
	v_fma_f32 v13, v165, v13, v51
	s_sub_i32 s12, 0x79, s20
	s_add_i32 s14, s20, 6
	v_mfma_f32_16x16x32_bf16 v[10:13], v[154:157], v[174:177], v[10:13]
	s_and_b64 s[2:3], s[6:7], exec
	s_cselect_b32 s2, s14, s12
	s_add_i32 s2, s2, s21
	v_mfma_f32_16x16x32_bf16 v[150:153], v[150:153], v[170:173], v[10:13]
	s_waitcnt lgkmcnt(0)
	s_mov_b64 s[98:99], exec
	s_mov_b64 exec, s[0:1]
	ds_write_b32 v222, v223
	s_mov_b64 exec, s[98:99]
	ds_read_b32 v230, v231
	s_ashr_i32 s3, s2, 31
	s_lshl_b64 s[12:13], s[2:3], 13
	s_add_u32 s26, s22, s12
	s_waitcnt vmcnt(36)
	v_lshlrev_b32_e32 v10, 16, v214
	v_and_b32_e32 v11, 0xffff0000, v214
	v_fma_f32 v2, v46, v2, v10
	v_fma_f32 v3, v47, v3, v11
	v_lshlrev_b32_e32 v10, 16, v215
	v_and_b32_e32 v11, 0xffff0000, v215
	v_fma_f32 v4, v48, v4, v10
	v_fma_f32 v5, v49, v5, v11
	s_addc_u32 s27, s23, s13
	s_lshl_b64 s[2:3], s[2:3], 8
	v_mfma_f32_16x16x32_bf16 v[2:5], v[34:37], v[174:177], v[2:5]
	s_cmp_lt_u32 s20, 4
	v_mfma_f32_16x16x32_bf16 v[50:53], v[38:41], v[170:173], v[2:5]
	s_waitcnt vmcnt(35)
	s_nop 4
	v_lshlrev_b32_e32 v2, 16, v210
	v_and_b32_e32 v3, 0xffff0000, v210
	v_lshlrev_b32_e32 v4, 16, v211
	v_and_b32_e32 v5, 0xffff0000, v211
	s_waitcnt vmcnt(33)
	v_fma_f32 v2, v42, v6, v2
	v_fma_f32 v3, v43, v7, v3
	v_fma_f32 v4, v44, v8, v4
	v_fma_f32 v5, v45, v9, v5
	v_lshl_add_u64 v[6:7], v[190:191], 0, s[2:3]
	v_lshl_add_u64 v[8:9], v[192:193], 0, s[12:13]
	v_mfma_f32_16x16x32_bf16 v[2:5], v[26:29], v[174:177], v[2:5]
	global_load_dwordx4 v[42:45], v186, s[26:27]
	global_load_dwordx4 v[34:37], v186, s[26:27] offset:1024
	v_mfma_f32_16x16x32_bf16 v[98:101], v[30:33], v[170:173], v[2:5]
	s_nop 4
	v_lshlrev_b32_e32 v2, 16, v196
	v_and_b32_e32 v3, 0xffff0000, v196
	v_lshlrev_b32_e32 v4, 16, v197
	v_and_b32_e32 v5, 0xffff0000, v197
	s_waitcnt vmcnt(34)
	v_fma_f32 v2, v22, v14, v2
	v_fma_f32 v3, v23, v15, v3
	v_fma_f32 v4, v24, v16, v4
	v_fma_f32 v5, v25, v17, v5
	s_nop 1
	v_mfma_f32_16x16x32_bf16 v[154:157], v[18:21], v[174:177], v[2:5]
	global_load_dwordx4 v[18:21], v186, s[26:27] offset:2048
	global_load_dwordx4 v[22:25], v186, s[26:27] offset:3072
	global_load_dwordx4 v[46:49], v[6:7], off
	global_load_dwordx4 v[26:29], v[6:7], off offset:64
	v_lshl_add_u64 v[2:3], s[26:27], 0, v[186:187]
	v_add_co_u32_e32 v2, vcc, 0x1000, v2
	v_mfma_f32_16x16x32_bf16 v[162:165], v[102:105], v[170:173], v[154:157]
	s_nop 0
	v_addc_co_u32_e32 v3, vcc, 0, v3, vcc
	global_load_dwordx4 v[38:41], v220, s[26:27]
	global_load_dwordx4 v[14:17], v221, s[26:27]
	global_load_dwordx4 v[10:13], v[2:3], off offset:1024
	s_nop 0
	global_load_dwordx4 v[2:5], v[2:3], off offset:3072
	s_nop 0
	global_load_dwordx2 v[196:197], v[8:9], off
	global_load_dwordx2 v[184:185], v[8:9], off offset:512
	global_load_dwordx2 v[182:183], v[8:9], off offset:1024
	global_load_dwordx2 v[194:195], v[8:9], off offset:1536
	global_load_dwordx4 v[30:33], v[6:7], off offset:128
	s_nop 0
	global_load_dwordx4 v[6:9], v[6:7], off offset:192
	s_cbranch_scc1 .LBB0_3643
	s_add_i32 s12, s9, 0
	s_add_i32 s12, s12, 0x10020
	s_waitcnt lgkmcnt(0)
	v_add_u32_e32 v102, 8, v230
	v_cmp_lt_u32_e32 vcc, s15, v102
	s_cbranch_vccnz .LBB0_3643

.LBB0_3643:
	s_lshl_b32 s2, s15, 11
	s_and_b32 s2, s2, 0x3000
	v_add_u32_e32 v102, s2, v189
	v_cvt_pk_bf16_f32 v170, v150, v151
	v_cvt_pk_bf16_f32 v171, v152, v153
	v_cvt_pk_bf16_f32 v172, v50, v51
	v_cvt_pk_bf16_f32 v173, v52, v53
	v_cvt_pk_bf16_f32 v154, v98, v99
	v_cvt_pk_bf16_f32 v155, v100, v101
	v_cvt_pk_bf16_f32 v156, v162, v163
	v_cvt_pk_bf16_f32 v157, v164, v165
	ds_write2st64_b64 v102, v[170:171], v[172:173] offset1:1
	ds_write2st64_b64 v102, v[154:155], v[156:157] offset0:2 offset1:3
	s_nop 1
	v_mov_b32_e32 v222, s9
	v_add_u32_e32 v222, 0x10000, v222
	v_add_u32_e32 v231, 32, v222
	v_mov_b32_e32 v223, s16
	s_waitcnt vmcnt(37)
	v_lshlrev_b32_e32 v102, 16, v202
	v_and_b32_e32 v103, 0xffff0000, v202
	v_fma_f32 v94, v94, v150, v102
	v_fma_f32 v95, v95, v151, v103
	v_lshlrev_b32_e32 v102, 16, v203
	v_and_b32_e32 v103, 0xffff0000, v203
	v_fma_f32 v96, v96, v152, v102
	v_fma_f32 v97, v97, v153, v103
	s_sub_i32 s12, 0x78, s20
	s_add_i32 s13, s20, 7
	v_mfma_f32_16x16x32_bf16 v[90:93], v[90:93], v[170:173], v[94:97]
	s_and_b64 s[2:3], s[6:7], exec
	s_cselect_b32 s2, s13, s12
	s_add_i32 s2, s2, s21
	v_mfma_f32_16x16x32_bf16 v[150:153], v[86:89], v[154:157], v[90:93]
	s_waitcnt lgkmcnt(0)
	s_mov_b64 s[98:99], exec
	s_mov_b64 exec, s[0:1]
	ds_write_b32 v222, v223
	s_mov_b64 exec, s[98:99]
	ds_read_b32 v230, v231
	s_waitcnt vmcnt(36)
	v_lshlrev_b32_e32 v86, 16, v200
	v_and_b32_e32 v87, 0xffff0000, v200
	v_fma_f32 v50, v82, v50, v86
	v_fma_f32 v51, v83, v51, v87
	v_lshlrev_b32_e32 v82, 16, v201
	v_and_b32_e32 v83, 0xffff0000, v201
	v_fma_f32 v52, v84, v52, v82
	v_fma_f32 v53, v85, v53, v83
	s_ashr_i32 s3, s2, 31
	s_lshl_b64 s[12:13], s[2:3], 13
	v_mfma_f32_16x16x32_bf16 v[50:53], v[70:73], v[170:173], v[50:53]
	s_add_u32 s26, s22, s12
	s_addc_u32 s27, s23, s13
	s_lshl_b64 s[2:3], s[2:3], 8
	v_mfma_f32_16x16x32_bf16 v[102:105], v[74:77], v[154:157], v[50:53]
	v_lshl_add_u64 v[74:75], v[190:191], 0, s[2:3]
	v_lshl_add_u64 v[76:77], v[192:193], 0, s[12:13]
	s_cmp_lt_u32 s20, 3
	s_waitcnt vmcnt(35)
	v_lshlrev_b32_e32 v50, 16, v198
	v_and_b32_e32 v51, 0xffff0000, v198
	v_lshlrev_b32_e32 v52, 16, v199
	v_and_b32_e32 v53, 0xffff0000, v199
	s_waitcnt vmcnt(33)
	v_fma_f32 v50, v78, v98, v50
	v_fma_f32 v51, v79, v99, v51
	v_fma_f32 v52, v80, v100, v52
	v_fma_f32 v53, v81, v101, v53
	global_load_dwordx4 v[86:89], v186, s[26:27]
	global_load_dwordx4 v[78:81], v186, s[26:27] offset:1024
	v_mfma_f32_16x16x32_bf16 v[50:53], v[62:65], v[170:173], v[50:53]
	v_mfma_f32_16x16x32_bf16 v[98:101], v[66:69], v[154:157], v[50:53]
	global_load_dwordx4 v[62:65], v186, s[26:27] offset:2048
	global_load_dwordx4 v[66:69], v186, s[26:27] offset:3072
	global_load_dwordx4 v[94:97], v[74:75], off
	global_load_dwordx4 v[82:85], v[74:75], off offset:64
	s_nop 2
	v_lshlrev_b32_e32 v50, 16, v178
	v_and_b32_e32 v51, 0xffff0000, v178
	v_lshlrev_b32_e32 v52, 16, v179
	v_and_b32_e32 v53, 0xffff0000, v179
	s_waitcnt vmcnt(38)
	v_fma_f32 v50, v58, v162, v50
	v_fma_f32 v51, v59, v163, v51
	v_fma_f32 v52, v60, v164, v52
	v_fma_f32 v53, v61, v165, v53
	s_nop 1
	v_mfma_f32_16x16x32_bf16 v[162:165], v[54:57], v[170:173], v[50:53]
	s_nop 2
	v_lshl_add_u64 v[50:51], s[26:27], 0, v[186:187]
	v_add_co_u32_e32 v50, vcc, 0x1000, v50
	v_mfma_f32_16x16x32_bf16 v[106:109], v[106:109], v[154:157], v[162:165]
	s_nop 0
	v_addc_co_u32_e32 v51, vcc, 0, v51, vcc
	global_load_dwordx4 v[58:61], v220, s[26:27]
	global_load_dwordx4 v[54:57], v221, s[26:27]
	global_load_dwordx4 v[70:73], v[50:51], off offset:1024
	s_nop 0
	global_load_dwordx4 v[50:53], v[50:51], off offset:3072
	s_nop 0
	global_load_dwordx2 v[204:205], v[76:77], off
	global_load_dwordx2 v[202:203], v[76:77], off offset:512
	global_load_dwordx2 v[200:201], v[76:77], off offset:1024
	global_load_dwordx2 v[198:199], v[76:77], off offset:1536
	global_load_dwordx4 v[90:93], v[74:75], off offset:128
	s_nop 0
	global_load_dwordx4 v[74:77], v[74:75], off offset:192
	s_cbranch_scc1 .LBB0_3648
	s_add_i32 s12, s9, 0
	s_add_i32 s12, s12, 0x10020
	s_waitcnt lgkmcnt(0)
	v_add_u32_e32 v154, 8, v230
	v_cmp_lt_u32_e32 vcc, s16, v154
	s_cbranch_vccnz .LBB0_3648

.LBB0_3648:
	s_lshl_b32 s2, s16, 11
	s_and_b32 s2, s2, 0x3800
	v_add_u32_e32 v154, s2, v189
	v_cvt_pk_bf16_f32 v170, v150, v151
	v_cvt_pk_bf16_f32 v171, v152, v153
	v_cvt_pk_bf16_f32 v172, v102, v103
	v_cvt_pk_bf16_f32 v173, v104, v105
	v_cvt_pk_bf16_f32 v162, v98, v99
	v_cvt_pk_bf16_f32 v163, v100, v101
	v_cvt_pk_bf16_f32 v164, v106, v107
	v_cvt_pk_bf16_f32 v165, v108, v109
	ds_write2st64_b64 v154, v[170:171], v[172:173] offset1:1
	ds_write2st64_b64 v154, v[162:163], v[164:165] offset0:2 offset1:3
	s_nop 1
	v_mov_b32_e32 v222, s9
	v_add_u32_e32 v222, 0x10000, v222
	v_add_u32_e32 v231, 32, v222
	v_mov_b32_e32 v223, s14
	s_waitcnt vmcnt(37)
	v_lshlrev_b32_e32 v154, 16, v212
	v_and_b32_e32 v155, 0xffff0000, v212
	v_fma_f32 v150, v166, v150, v154
	v_fma_f32 v151, v167, v151, v155
	v_lshlrev_b32_e32 v154, 16, v213
	v_and_b32_e32 v155, 0xffff0000, v213
	v_fma_f32 v152, v168, v152, v154
	v_fma_f32 v153, v169, v153, v155
	s_cmpk_lt_u32 s20, 0x78
	s_nop 0
	v_mfma_f32_16x16x32_bf16 v[150:153], v[158:161], v[170:173], v[150:153]
	v_mfma_f32_16x16x32_bf16 v[154:157], v[146:149], v[162:165], v[150:153]
	s_waitcnt lgkmcnt(0)
	s_mov_b64 s[98:99], exec
	s_mov_b64 exec, s[0:1]
	ds_write_b32 v222, v223
	s_mov_b64 exec, s[98:99]
	ds_read_b32 v230, v231
	s_waitcnt vmcnt(36)
	v_lshlrev_b32_e32 v146, 16, v208
	v_and_b32_e32 v147, 0xffff0000, v208
	v_fma_f32 v102, v142, v102, v146
	v_fma_f32 v103, v143, v103, v147
	v_lshlrev_b32_e32 v142, 16, v209
	v_and_b32_e32 v143, 0xffff0000, v209
	v_fma_f32 v104, v144, v104, v142
	v_fma_f32 v105, v145, v105, v143
	s_nop 1
	v_mfma_f32_16x16x32_bf16 v[102:105], v[130:133], v[170:173], v[102:105]
	v_mfma_f32_16x16x32_bf16 v[150:153], v[134:137], v[162:165], v[102:105]
	s_waitcnt vmcnt(35)
	s_nop 5
	v_lshlrev_b32_e32 v102, 16, v206
	v_and_b32_e32 v103, 0xffff0000, v206
	s_waitcnt vmcnt(33)
	v_fma_f32 v98, v138, v98, v102
	v_fma_f32 v99, v139, v99, v103
	v_lshlrev_b32_e32 v102, 16, v207
	v_and_b32_e32 v103, 0xffff0000, v207
	v_fma_f32 v100, v140, v100, v102
	v_fma_f32 v101, v141, v101, v103
	s_nop 1
	v_mfma_f32_16x16x32_bf16 v[98:101], v[122:125], v[170:173], v[98:101]
	v_mfma_f32_16x16x32_bf16 v[102:105], v[126:129], v[162:165], v[98:101]
	s_nop 6
	v_lshlrev_b32_e32 v98, 16, v180
	v_and_b32_e32 v99, 0xffff0000, v180
	v_lshlrev_b32_e32 v100, 16, v181
	v_and_b32_e32 v101, 0xffff0000, v181
	s_waitcnt vmcnt(32)
	v_fma_f32 v98, v118, v106, v98
	v_fma_f32 v99, v119, v107, v99
	v_fma_f32 v100, v120, v108, v100
	v_fma_f32 v101, v121, v109, v101
	s_nop 1
	v_mfma_f32_16x16x32_bf16 v[98:101], v[114:117], v[170:173], v[98:101]
	v_mfma_f32_16x16x32_bf16 v[106:109], v[110:113], v[162:165], v[98:101]
	s_cbranch_scc0 .LBB0_3652
	s_mov_b32 s20, s14
	s_branch .LBB0_3620

.LBB0_3655:
	v_cvt_pk_bf16_f32 v50, v154, v155
	v_cvt_pk_bf16_f32 v51, v156, v157
	v_cvt_pk_bf16_f32 v52, v150, v151
	v_cvt_pk_bf16_f32 v53, v152, v153
	v_cvt_pk_bf16_f32 v54, v102, v103
	v_cvt_pk_bf16_f32 v55, v104, v105
	v_cvt_pk_bf16_f32 v56, v106, v107
	v_cvt_pk_bf16_f32 v57, v108, v109
	ds_write2st64_b64 v189, v[50:51], v[52:53] offset0:24 offset1:25
	ds_write2st64_b64 v189, v[54:55], v[56:57] offset0:26 offset1:27
	s_waitcnt lgkmcnt(0)
	s_and_saveexec_b64 s[6:7], s[0:1]
	s_add_i32 s2, s12, 0x10000
	v_mov_b32_e32 v58, 0x7f
	v_mov_b32_e32 v59, s2
	ds_write_b32 v59, v58
	s_or_b64 exec, exec, s[6:7]
	v_lshlrev_b32_e32 v58, 16, v196
	v_and_b32_e32 v59, 0xffff0000, v196
	v_fma_f32 v46, v46, v154, v58
	v_fma_f32 v47, v47, v155, v59
	v_lshlrev_b32_e32 v58, 16, v197
	v_and_b32_e32 v59, 0xffff0000, v197
	v_fma_f32 v48, v48, v156, v58
	v_fma_f32 v49, v49, v157, v59
	s_movk_i32 s2, 0xff80
	s_nop 0
	v_mfma_f32_16x16x32_bf16 v[42:45], v[42:45], v[50:53], v[46:49]
	v_mfma_f32_16x16x32_bf16 v[34:37], v[34:37], v[54:57], v[42:45]
	s_nop 6
	v_lshlrev_b32_e32 v42, 16, v184
	v_and_b32_e32 v43, 0xffff0000, v184
	v_fma_f32 v26, v26, v150, v42
	v_fma_f32 v27, v27, v151, v43
	v_lshlrev_b32_e32 v42, 16, v185
	v_and_b32_e32 v43, 0xffff0000, v185
	v_fma_f32 v28, v28, v152, v42
	v_fma_f32 v29, v29, v153, v43
	s_nop 1
	v_mfma_f32_16x16x32_bf16 v[18:21], v[18:21], v[50:53], v[26:29]
	v_mfma_f32_16x16x32_bf16 v[18:21], v[22:25], v[54:57], v[18:21]
	v_lshlrev_b32_e32 v22, 16, v182
	v_and_b32_e32 v23, 0xffff0000, v182
	v_lshlrev_b32_e32 v24, 16, v183
	v_and_b32_e32 v25, 0xffff0000, v183
	v_fma_f32 v22, v30, v102, v22
	v_fma_f32 v23, v31, v103, v23
	v_fma_f32 v24, v32, v104, v24
	v_fma_f32 v25, v33, v105, v25
	s_nop 1
	v_mfma_f32_16x16x32_bf16 v[22:25], v[38:41], v[50:53], v[22:25]
	v_mfma_f32_16x16x32_bf16 v[10:13], v[10:13], v[54:57], v[22:25]
	s_nop 6
	v_lshlrev_b32_e32 v22, 16, v194
	v_and_b32_e32 v23, 0xffff0000, v194
	v_fma_f32 v6, v6, v106, v22
	v_fma_f32 v7, v7, v107, v23
	v_mov_b32_e32 v22, s13
	ds_read_b32 v24, v22
	v_lshlrev_b32_e32 v22, 16, v195
	v_and_b32_e32 v23, 0xffff0000, v195
	v_fma_f32 v8, v8, v108, v22
	v_fma_f32 v9, v9, v109, v23
	s_nop 1
	v_mfma_f32_16x16x32_bf16 v[6:9], v[14:17], v[50:53], v[6:9]
	s_waitcnt lgkmcnt(0)
	v_add_u32_e32 v14, 0xffffff88, v24
	v_cmp_gt_u32_e32 vcc, s2, v14
	v_mfma_f32_16x16x32_bf16 v[2:5], v[2:5], v[54:57], v[6:9]
	s_cbranch_vccnz .LBB0_3660
	s_movk_i32 s6, 0xff7f
